# weight-conversion split between the w_in phase and the router phase moved from 90/10 to 85/15 (router workgroups skip the pool, so the pool half of that phase had slack)
# speedup vs baseline: 1.0065x; 1.0054x over previous
; DI CvItem cv_decode(const Params& P, int it) { CvItem c; int item;
;     if (it < NE * CV_GU1) { const int e = it / CV_GU1; c.W = P.in[I_WGU] + (size_t)e * D * 4096; c.N = 4096; c.WT = (unsigned char*)(P.ws + WS_WGU) + (size_t)e * 4096 * D; c.kind = 2; item = it % CV_GU1; }
;     else { const int r = it - NE * CV_GU1; const int e = r / CV_DN1; c.W = P.in[I_WDN] + (size_t)e * D * D; c.N = D; c.WT = (unsigned char*)(P.ws + WS_WDN) + (size_t)e * D * D; c.kind = 3; item = r % CV_DN1; }
;     const int nblk = c.N / 32, kb = item / nblk, nb = item % nblk; c.k0 = 128 * kb; c.n0 = 32 * nb; return c; }
; DI void conv_pool(const Params& P, LAS unsigned char* lds, int pool, int blk_lo, int blk_hi) {
;     ...
;     auto claim = [&]() -> int { unsigned v_ = 0u; if (lane == 0) v_ = __hip_atomic_fetch_add(ctr, 1u, __ATOMIC_RELAXED, __HIP_MEMORY_SCOPE_AGENT); return blk_lo + (int)__builtin_amdgcn_readfirstlane(v_); };
;     const int blk = claim(); if (blk >= CV_NBLK) return;
;     int it = blk * CV_BLK, left = CV_BLK;
;     CvItem cur = cv_decode(P, it); f32x4 v[16]; cv_issue(cur, lane, v);
.LBB0_363:
	s_or_b64 exec, exec, s[2:3]
	v_readfirstlane_b32 s13, v0
	s_cmpk_gt_i32 s13, 0x28cc
	s_cbranch_scc1 .LBB0_383
	s_lshl_b32 s38, s13, 3
	s_cmpk_gt_i32 s13, 0x1fff
	s_mov_b32 s11, 3
	s_cbranch_scc0 .LBB0_366
	s_add_i32 s2, s38, 0xffff0000
	s_lshr_b32 s2, s2, 10
	s_mov_b32 s3, 0
	v_readlane_b32 s48, v254, 6
	s_lshl_b64 s[6:7], s[2:3], 22
	s_lshl_b64 s[2:3], s[2:3], 24
	v_readlane_b32 s50, v254, 8
	v_readlane_b32 s51, v254, 9
	s_add_u32 s14, s50, s2
	v_readlane_b32 s40, v254, 2
	s_addc_u32 s15, s51, s3
	v_readlane_b32 s42, v254, 4
	v_readlane_b32 s43, v254, 5
	s_add_u32 s2, s42, s6
	s_addc_u32 s3, s43, s7
	s_add_u32 s6, s2, 0x12400000
	v_readlane_b32 s49, v254, 7
	v_readlane_b32 s52, v254, 10
	v_readlane_b32 s53, v254, 11
	v_readlane_b32 s54, v254, 12
	v_readlane_b32 s55, v254, 13
	v_readlane_b32 s41, v254, 3
	s_addc_u32 s7, s3, 0
	s_and_b32 s10, s38, 0x3f8
	s_movk_i32 s16, 0x800
	s_cbranch_execz .LBB0_367
	s_branch .LBB0_368

; DI void conv_pool(const Params& P, LAS unsigned char* lds, int pool, int blk_lo, int blk_hi) {
;     ...
;     for (;;) { int nx = it + 1; bool more = true;
;     ...
;         const CvItem nxt = cv_decode(P, nx); f32x4 vn[16]; cv_issue(nxt, lane, vn);
.LBB0_376:
	s_or_b64 exec, exec, s[2:3]
	v_readfirstlane_b32 s2, v56
	s_lshl_b32 s22, s2, 3
	s_cmpk_lt_i32 s2, 0x28cd
	s_cselect_b64 s[2:3], -1, 0
	s_and_b64 s[16:17], s[2:3], exec
	s_cselect_b32 s43, 8, s14
	s_cselect_b32 s44, s22, s38
	s_branch .LBB0_379

; DI CvItem cv_decode(const Params& P, int it) { CvItem c; int item;
;     if (it < NE * CV_GU1) { const int e = it / CV_GU1; c.W = P.in[I_WGU] + (size_t)e * D * 4096; c.N = 4096; c.WT = (unsigned char*)(P.ws + WS_WGU) + (size_t)e * 4096 * D; c.kind = 2; item = it % CV_GU1; }
;     else { const int r = it - NE * CV_GU1; const int e = r / CV_DN1; c.W = P.in[I_WDN] + (size_t)e * D * D; c.N = D; c.WT = (unsigned char*)(P.ws + WS_WDN) + (size_t)e * D * D; c.kind = 3; item = r % CV_DN1; }
;     const int nblk = c.N / 32, kb = item / nblk, nb = item % nblk; c.k0 = 128 * kb; c.n0 = 32 * nb; return c; }
; DI void conv_pool(const Params& P, LAS unsigned char* lds, int pool, int blk_lo, int blk_hi) {
;     ...
;     auto claim = [&]() -> int { unsigned v_ = 0u; if (lane == 0) v_ = __hip_atomic_fetch_add(ctr, 1u, __ATOMIC_RELAXED, __HIP_MEMORY_SCOPE_AGENT); return blk_lo + (int)__builtin_amdgcn_readfirstlane(v_); };
;     const int blk = claim(); if (blk >= CV_NBLK) return;
;     int it = blk * CV_BLK, left = CV_BLK;
;     CvItem cur = cv_decode(P, it); f32x4 v[16]; cv_issue(cur, lane, v);
.LBB0_1116:
	s_or_b64 exec, exec, s[2:3]
	v_readfirstlane_b32 s2, v0
	s_cmpk_gt_i32 s2, 0x732
	s_cbranch_scc1 .LBB0_1136
	s_add_i32 s13, s2, 0x28cd
	s_lshl_b32 s20, s13, 3
	s_cmpk_gt_i32 s2, 0xf732
	s_mov_b32 s11, 3
	s_cbranch_scc0 .LBB0_1119
	s_add_i32 s2, s20, 0xffff0000
	v_readlane_b32 s36, v254, 6
	s_lshr_b32 s2, s2, 10
	s_mov_b32 s3, 0
	v_readlane_b32 s38, v254, 8
	v_readlane_b32 s39, v254, 9
	s_lshl_b64 s[6:7], s[2:3], 22
	s_lshl_b64 s[2:3], s[2:3], 24
	s_mov_b64 s[14:15], s[38:39]
	s_add_u32 s14, s14, s2
	v_readlane_b32 s16, v254, 2
	s_addc_u32 s15, s15, s3
	v_readlane_b32 s18, v254, 4
	v_readlane_b32 s19, v254, 5
	s_add_u32 s2, s18, s6
	s_addc_u32 s3, s19, s7
	s_add_u32 s6, s2, 0x12400000
	v_readlane_b32 s37, v254, 7
	v_readlane_b32 s40, v254, 10
	v_readlane_b32 s41, v254, 11
	v_readlane_b32 s42, v254, 12
	v_readlane_b32 s43, v254, 13
	v_readlane_b32 s17, v254, 3
	s_addc_u32 s7, s3, 0
	s_and_b32 s10, s20, 0x3f8
	s_movk_i32 s16, 0x800
	s_cbranch_execz .LBB0_1120
	s_branch .LBB0_1121

; DI void conv_pool(const Params& P, LAS unsigned char* lds, int pool, int blk_lo, int blk_hi) {
;     ...
;     for (;;) { int nx = it + 1; bool more = true;
;     ...
;         const CvItem nxt = cv_decode(P, nx); f32x4 vn[16]; cv_issue(nxt, lane, vn);
.LBB0_1129:
	s_or_b64 exec, exec, s[2:3]
	v_readfirstlane_b32 s2, v56
	s_lshl_b32 s3, s2, 3
	s_add_i32 s18, s3, 0x14668
	s_cmpk_lt_i32 s2, 0x733
	s_cselect_b64 s[2:3], -1, 0
	s_and_b64 s[16:17], s[2:3], exec
	s_cselect_b32 s28, 8, s14
	s_cselect_b32 s29, s18, s20
	s_branch .LBB0_1132
